# v25: v21 + grid barrier acquire (buffer_inv sc1) issued at arrival instead of after the release
# speedup vs baseline: 1.0053x; 1.0017x over previous
.LBB0_274:
	s_or_b64 exec, exec, s[4:5]
	v_cvt_f32_u32_e32 v5, v3
	s_waitcnt vmcnt(0)
	v_readfirstlane_b32 s0, v4
	v_sub_u32_e32 v4, 0, v3
	v_rcp_iflag_f32_e32 v5, v5
	v_add_u32_e32 v6, s0, v1
	v_mul_f32_e32 v5, 0x4f7ffffe, v5
	v_cvt_u32_f32_e32 v5, v5
	v_mul_lo_u32 v1, v4, v5
	v_mul_hi_u32 v1, v5, v1
	v_add_u32_e32 v1, v5, v1
	v_mul_hi_u32 v1, v6, v1
	v_mul_lo_u32 v4, v1, v3
	v_sub_u32_e32 v4, v6, v4
	v_add_u32_e32 v5, 1, v1
	v_cmp_ge_u32_e32 vcc, v4, v3
	s_nop 1
	v_cndmask_b32_e32 v1, v1, v5, vcc
	v_sub_u32_e32 v5, v4, v3
	v_cndmask_b32_e32 v4, v4, v5, vcc
	v_add_u32_e32 v5, 1, v1
	v_cmp_ge_u32_e32 vcc, v4, v3
	v_add_u32_e32 v4, 1, v6
	s_nop 0
	v_cndmask_b32_e32 v1, v1, v5, vcc
	v_mul_lo_u32 v5, v3, v1
	v_add_u32_e32 v3, v5, v3
	v_cmp_ne_u32_e32 vcc, v4, v3
	s_and_saveexec_b64 s[0:1], vcc
	s_xor_b64 s[4:5], exec, s[0:1]
	s_cbranch_execz .LBB0_288
	buffer_inv sc1
	v_readlane_b32 s0, v251, 17
	v_readlane_b32 s1, v251, 18
	s_waitcnt lgkmcnt(0)
	s_nop 3
	global_load_dword v2, v203, s[0:1] sc1
	s_waitcnt vmcnt(0)
	v_cmp_eq_u32_e32 vcc, v2, v1
	s_and_saveexec_b64 s[6:7], vcc
	s_cbranch_execz .LBB0_287
	s_mov_b32 s0, 1
	s_mov_b64 s[8:9], 0
	s_branch .LBB0_278

.LBB0_287:
	s_or_b64 exec, exec, s[6:7]
	s_waitcnt vmcnt(0)
	s_waitcnt vmcnt(0)
.LBB0_288:
	s_andn2_saveexec_b64 s[0:1], s[4:5]
	s_cbranch_execz .LBB0_308
	s_mov_b64 s[4:5], exec
	buffer_wbl2 sc1
	buffer_inv sc1
	s_waitcnt lgkmcnt(0)
	s_waitcnt vmcnt(0)
	v_mbcnt_lo_u32_b32 v1, s4, 0
	v_mbcnt_hi_u32_b32 v1, s5, v1
	v_cmp_eq_u32_e32 vcc, 0, v1
	s_and_saveexec_b64 s[6:7], vcc
	s_cbranch_execz .LBB0_291
	s_bcnt1_i32_b64 s0, s[4:5]
	v_mov_b32_e32 v3, s0
	v_readlane_b32 s0, v251, 19
	v_readlane_b32 s1, v251, 20
	s_nop 4
	global_atomic_add v3, v203, v3, s[0:1] sc0

.LBB0_305:
	s_or_b64 exec, exec, s[4:5]
	s_mov_b64 s[4:5], exec
	v_mbcnt_lo_u32_b32 v1, s4, 0
	v_mbcnt_hi_u32_b32 v1, s5, v1
	v_cmp_eq_u32_e32 vcc, 0, v1
	s_waitcnt vmcnt(0)
	s_and_saveexec_b64 s[6:7], vcc
	s_cbranch_execz .LBB0_307
	s_bcnt1_i32_b64 s0, s[4:5]
	v_mov_b32_e32 v1, s0
	v_readlane_b32 s0, v251, 17
	v_readlane_b32 s1, v251, 18
	s_nop 4
	global_atomic_add v203, v1, s[0:1]

.LBB0_402:
	s_or_b64 exec, exec, s[4:5]
	v_cvt_f32_u32_e32 v5, v3
	s_waitcnt vmcnt(0)
	v_readfirstlane_b32 s1, v4
	v_sub_u32_e32 v4, 0, v3
	v_rcp_iflag_f32_e32 v5, v5
	v_add_u32_e32 v6, s1, v1
	v_mul_f32_e32 v5, 0x4f7ffffe, v5
	v_cvt_u32_f32_e32 v5, v5
	v_mul_lo_u32 v1, v4, v5
	v_mul_hi_u32 v1, v5, v1
	v_add_u32_e32 v1, v5, v1
	v_mul_hi_u32 v1, v6, v1
	v_mul_lo_u32 v4, v1, v3
	v_sub_u32_e32 v4, v6, v4
	v_add_u32_e32 v5, 1, v1
	v_cmp_ge_u32_e32 vcc, v4, v3
	s_nop 1
	v_cndmask_b32_e32 v1, v1, v5, vcc
	v_sub_u32_e32 v5, v4, v3
	v_cndmask_b32_e32 v4, v4, v5, vcc
	v_add_u32_e32 v5, 1, v1
	v_cmp_ge_u32_e32 vcc, v4, v3
	v_add_u32_e32 v4, 1, v6
	s_nop 0
	v_cndmask_b32_e32 v1, v1, v5, vcc
	v_mul_lo_u32 v5, v3, v1
	v_add_u32_e32 v3, v5, v3
	v_cmp_ne_u32_e32 vcc, v4, v3
	s_and_saveexec_b64 s[4:5], vcc
	s_xor_b64 s[4:5], exec, s[4:5]
	s_cbranch_execz .LBB0_416
	buffer_inv sc1
	v_readlane_b32 s6, v251, 17
	v_readlane_b32 s7, v251, 18
	s_waitcnt lgkmcnt(0)
	s_nop 3
	global_load_dword v2, v203, s[6:7] sc1
	s_waitcnt vmcnt(0)
	v_cmp_eq_u32_e32 vcc, v2, v1
	s_and_saveexec_b64 s[6:7], vcc
	s_cbranch_execz .LBB0_415
	s_mov_b32 s1, 1
	s_mov_b64 s[8:9], 0
	s_branch .LBB0_406

.LBB0_416:
	s_andn2_saveexec_b64 s[4:5], s[4:5]
	s_cbranch_execz .LBB0_436
	s_mov_b64 s[4:5], exec
	buffer_wbl2 sc1
	buffer_inv sc1
	s_waitcnt lgkmcnt(0)
	s_waitcnt vmcnt(0)
	v_mbcnt_lo_u32_b32 v1, s4, 0
	v_mbcnt_hi_u32_b32 v1, s5, v1
	v_cmp_eq_u32_e32 vcc, 0, v1
	s_and_saveexec_b64 s[6:7], vcc
	s_cbranch_execz .LBB0_419
	s_bcnt1_i32_b64 s1, s[4:5]
	v_readlane_b32 s4, v251, 19
	v_mov_b32_e32 v3, s1
	v_readlane_b32 s5, v251, 20
	s_nop 4
	global_atomic_add v3, v203, v3, s[4:5] sc0

.LBB0_433:
	s_or_b64 exec, exec, s[4:5]
	s_mov_b64 s[4:5], exec
	v_mbcnt_lo_u32_b32 v1, s4, 0
	v_mbcnt_hi_u32_b32 v1, s5, v1
	v_cmp_eq_u32_e32 vcc, 0, v1
	s_waitcnt vmcnt(0)
	s_and_saveexec_b64 s[6:7], vcc
	s_cbranch_execz .LBB0_435
	s_bcnt1_i32_b64 s1, s[4:5]
	v_readlane_b32 s4, v251, 17
	v_mov_b32_e32 v1, s1
	v_readlane_b32 s5, v251, 18
	s_nop 4
	global_atomic_add v203, v1, s[4:5]

.LBB0_512:
	s_or_b64 exec, exec, s[4:5]
	v_cvt_f32_u32_e32 v5, v3
	s_waitcnt vmcnt(0)
	v_readfirstlane_b32 s0, v4
	v_sub_u32_e32 v4, 0, v3
	v_rcp_iflag_f32_e32 v5, v5
	v_add_u32_e32 v6, s0, v1
	v_mul_f32_e32 v5, 0x4f7ffffe, v5
	v_cvt_u32_f32_e32 v5, v5
	v_mul_lo_u32 v1, v4, v5
	v_mul_hi_u32 v1, v5, v1
	v_add_u32_e32 v1, v5, v1
	v_mul_hi_u32 v1, v6, v1
	v_mul_lo_u32 v4, v1, v3
	v_sub_u32_e32 v4, v6, v4
	v_add_u32_e32 v5, 1, v1
	v_cmp_ge_u32_e32 vcc, v4, v3
	s_nop 1
	v_cndmask_b32_e32 v1, v1, v5, vcc
	v_sub_u32_e32 v5, v4, v3
	v_cndmask_b32_e32 v4, v4, v5, vcc
	v_add_u32_e32 v5, 1, v1
	v_cmp_ge_u32_e32 vcc, v4, v3
	v_add_u32_e32 v4, 1, v6
	s_nop 0
	v_cndmask_b32_e32 v1, v1, v5, vcc
	v_mul_lo_u32 v5, v3, v1
	v_add_u32_e32 v3, v5, v3
	v_cmp_ne_u32_e32 vcc, v4, v3
	s_and_saveexec_b64 s[0:1], vcc
	s_xor_b64 s[4:5], exec, s[0:1]
	s_cbranch_execz .LBB0_526
	buffer_inv sc1
	v_readlane_b32 s0, v251, 17
	v_readlane_b32 s1, v251, 18
	s_waitcnt lgkmcnt(0)
	s_nop 3
	global_load_dword v2, v203, s[0:1] sc1
	s_waitcnt vmcnt(0)
	v_cmp_eq_u32_e32 vcc, v2, v1
	s_and_saveexec_b64 s[6:7], vcc
	s_cbranch_execz .LBB0_525
	s_mov_b32 s0, 1
	s_mov_b64 s[10:11], 0
	s_branch .LBB0_516

.LBB0_742:
	s_or_b64 exec, exec, s[4:5]
	v_cvt_f32_u32_e32 v5, v3
	s_waitcnt vmcnt(0)
	v_readfirstlane_b32 s1, v4
	v_sub_u32_e32 v4, 0, v3
	v_rcp_iflag_f32_e32 v5, v5
	v_add_u32_e32 v6, s1, v1
	v_mul_f32_e32 v5, 0x4f7ffffe, v5
	v_cvt_u32_f32_e32 v5, v5
	v_mul_lo_u32 v1, v4, v5
	v_mul_hi_u32 v1, v5, v1
	v_add_u32_e32 v1, v5, v1
	v_mul_hi_u32 v1, v6, v1
	v_mul_lo_u32 v4, v1, v3
	v_sub_u32_e32 v4, v6, v4
	v_add_u32_e32 v5, 1, v1
	v_cmp_ge_u32_e32 vcc, v4, v3
	s_nop 1
	v_cndmask_b32_e32 v1, v1, v5, vcc
	v_sub_u32_e32 v5, v4, v3
	v_cndmask_b32_e32 v4, v4, v5, vcc
	v_add_u32_e32 v5, 1, v1
	v_cmp_ge_u32_e32 vcc, v4, v3
	v_add_u32_e32 v4, 1, v6
	s_nop 0
	v_cndmask_b32_e32 v1, v1, v5, vcc
	v_mul_lo_u32 v5, v3, v1
	v_add_u32_e32 v3, v5, v3
	v_cmp_ne_u32_e32 vcc, v4, v3
	s_and_saveexec_b64 s[4:5], vcc
	s_xor_b64 s[4:5], exec, s[4:5]
	s_cbranch_execz .LBB0_756
	buffer_inv sc1
	v_readlane_b32 s8, v251, 17
	v_readlane_b32 s9, v251, 18
	s_waitcnt lgkmcnt(0)
	s_nop 3
	global_load_dword v2, v203, s[8:9] sc1
	s_waitcnt vmcnt(0)
	v_cmp_eq_u32_e32 vcc, v2, v1
	s_and_saveexec_b64 s[8:9], vcc
	s_cbranch_execz .LBB0_755
	s_mov_b32 s1, 1
	s_mov_b64 s[10:11], 0
	s_branch .LBB0_746

.LBB0_755:
	s_or_b64 exec, exec, s[8:9]
	s_waitcnt vmcnt(0)
	s_waitcnt vmcnt(0)
.LBB0_756:
	s_andn2_saveexec_b64 s[4:5], s[4:5]
	s_cbranch_execz .LBB0_776
	s_mov_b64 s[4:5], exec
	buffer_wbl2 sc1
	buffer_inv sc1
	s_waitcnt lgkmcnt(0)
	s_waitcnt vmcnt(0)
	v_mbcnt_lo_u32_b32 v1, s4, 0
	v_mbcnt_hi_u32_b32 v1, s5, v1
	v_cmp_eq_u32_e32 vcc, 0, v1
	s_and_saveexec_b64 s[8:9], vcc
	s_cbranch_execz .LBB0_759
	s_bcnt1_i32_b64 s1, s[4:5]
	v_readlane_b32 s4, v251, 19
	v_mov_b32_e32 v3, s1
	v_readlane_b32 s5, v251, 20
	s_nop 4
	global_atomic_add v3, v203, v3, s[4:5] sc0

.LBB0_773:
	s_or_b64 exec, exec, s[4:5]
	s_mov_b64 s[4:5], exec
	v_mbcnt_lo_u32_b32 v1, s4, 0
	v_mbcnt_hi_u32_b32 v1, s5, v1
	v_cmp_eq_u32_e32 vcc, 0, v1
	s_waitcnt vmcnt(0)
	s_and_saveexec_b64 s[8:9], vcc
	s_cbranch_execz .LBB0_775
	s_bcnt1_i32_b64 s1, s[4:5]
	v_readlane_b32 s4, v251, 17
	v_mov_b32_e32 v1, s1
	v_readlane_b32 s5, v251, 18
	s_nop 4
	global_atomic_add v203, v1, s[4:5]

.LBB0_1755:
	s_or_b64 exec, exec, s[8:9]
	v_cvt_f32_u32_e32 v5, v3
	s_waitcnt vmcnt(0)
	v_readfirstlane_b32 s0, v4
	v_sub_u32_e32 v4, 0, v3
	v_rcp_iflag_f32_e32 v5, v5
	v_add_u32_e32 v6, s0, v1
	v_mul_f32_e32 v5, 0x4f7ffffe, v5
	v_cvt_u32_f32_e32 v5, v5
	v_mul_lo_u32 v1, v4, v5
	v_mul_hi_u32 v1, v5, v1
	v_add_u32_e32 v1, v5, v1
	v_mul_hi_u32 v1, v6, v1
	v_mul_lo_u32 v4, v1, v3
	v_sub_u32_e32 v4, v6, v4
	v_add_u32_e32 v5, 1, v1
	v_cmp_ge_u32_e32 vcc, v4, v3
	s_nop 1
	v_cndmask_b32_e32 v1, v1, v5, vcc
	v_sub_u32_e32 v5, v4, v3
	v_cndmask_b32_e32 v4, v4, v5, vcc
	v_add_u32_e32 v5, 1, v1
	v_cmp_ge_u32_e32 vcc, v4, v3
	v_add_u32_e32 v4, 1, v6
	s_nop 0
	v_cndmask_b32_e32 v1, v1, v5, vcc
	v_mul_lo_u32 v5, v3, v1
	v_add_u32_e32 v3, v5, v3
	v_cmp_ne_u32_e32 vcc, v4, v3
	s_and_saveexec_b64 s[0:1], vcc
	s_xor_b64 s[8:9], exec, s[0:1]
	s_cbranch_execz .LBB0_1769
	buffer_inv sc1
	v_readlane_b32 s0, v251, 17
	v_readlane_b32 s1, v251, 18
	s_waitcnt lgkmcnt(0)
	s_nop 3
	global_load_dword v2, v203, s[0:1] sc1
	s_waitcnt vmcnt(0)
	v_cmp_eq_u32_e32 vcc, v2, v1
	s_and_saveexec_b64 s[12:13], vcc
	s_cbranch_execz .LBB0_1768
	s_mov_b32 s0, 1
	s_mov_b64 s[22:23], 0
	s_branch .LBB0_1759

.LBB0_1768:
	s_or_b64 exec, exec, s[12:13]
	s_waitcnt vmcnt(0)
	s_waitcnt vmcnt(0)
.LBB0_1769:
	s_andn2_saveexec_b64 s[0:1], s[8:9]
	s_cbranch_execz .LBB0_1789
	s_mov_b64 s[8:9], exec
	buffer_wbl2 sc1
	buffer_inv sc1
	s_waitcnt lgkmcnt(0)
	s_waitcnt vmcnt(0)
	v_mbcnt_lo_u32_b32 v1, s8, 0
	v_mbcnt_hi_u32_b32 v1, s9, v1
	v_cmp_eq_u32_e32 vcc, 0, v1
	s_and_saveexec_b64 s[12:13], vcc
	s_cbranch_execz .LBB0_1772
	s_bcnt1_i32_b64 s0, s[8:9]
	v_mov_b32_e32 v3, s0
	v_readlane_b32 s0, v251, 19
	v_readlane_b32 s1, v251, 20
	s_nop 4
	global_atomic_add v3, v203, v3, s[0:1] sc0

.LBB0_1786:
	s_or_b64 exec, exec, s[8:9]
	s_mov_b64 s[8:9], exec
	v_mbcnt_lo_u32_b32 v1, s8, 0
	v_mbcnt_hi_u32_b32 v1, s9, v1
	v_cmp_eq_u32_e32 vcc, 0, v1
	s_waitcnt vmcnt(0)
	s_and_saveexec_b64 s[12:13], vcc
	s_cbranch_execz .LBB0_1788
	s_bcnt1_i32_b64 s0, s[8:9]
	v_mov_b32_e32 v1, s0
	v_readlane_b32 s0, v251, 17
	v_readlane_b32 s1, v251, 18
	s_nop 4
	global_atomic_add v203, v1, s[0:1]

.LBB0_1920:
	s_or_b64 exec, exec, s[4:5]
	s_mov_b64 s[4:5], exec
	v_mbcnt_lo_u32_b32 v1, s4, 0
	v_mbcnt_hi_u32_b32 v1, s5, v1
	v_cmp_eq_u32_e32 vcc, 0, v1
	s_waitcnt vmcnt(0)
	s_and_saveexec_b64 s[6:7], vcc
	s_cbranch_execz .LBB0_1701
	s_bcnt1_i32_b64 s0, s[4:5]
	v_mov_b32_e32 v1, s0
	v_readlane_b32 s0, v251, 17
	v_readlane_b32 s1, v251, 18
	s_nop 4
	global_atomic_add v203, v1, s[0:1]
	s_branch .LBB0_1701

.LBB0_2130:
	s_mov_b64 s[4:5], exec
	buffer_wbl2 sc1
	buffer_inv sc1
	s_waitcnt lgkmcnt(0)
	s_waitcnt vmcnt(0)
	v_mbcnt_lo_u32_b32 v1, s4, 0
	v_mbcnt_hi_u32_b32 v1, s5, v1
	v_cmp_eq_u32_e32 vcc, 0, v1
	s_and_saveexec_b64 s[6:7], vcc
	s_cbranch_execz .LBB0_2132
	s_bcnt1_i32_b64 s0, s[4:5]
	v_mov_b32_e32 v3, s0
	v_readlane_b32 s0, v251, 19
	v_readlane_b32 s1, v251, 20
	s_nop 4
	global_atomic_add v3, v203, v3, s[0:1] sc0

.LBB0_2146:
	s_or_b64 exec, exec, s[4:5]
	s_mov_b64 s[4:5], exec
	v_mbcnt_lo_u32_b32 v1, s4, 0
	v_mbcnt_hi_u32_b32 v1, s5, v1
	v_cmp_eq_u32_e32 vcc, 0, v1
	s_waitcnt vmcnt(0)
	s_and_saveexec_b64 s[6:7], vcc
	s_cbranch_execnz .LBB0_2147
	s_getpc_b64 s[98:99]
